# indexer passes: the next tile's K fragments are requested after the second half's matrix ops instead of right in front of a wait that also covered them
# speedup vs baseline: 1.0121x; 1.0121x over previous
; __device__ __forceinline__ float relu_i(float p) { const int i = __float_as_int(p); return __int_as_float(i > 0 ? i : 0); }
; __device__ __forceinline__ void idx_scores_k(f32x16& sc, const bf16x8 (&kf)[4], const bf16x8 (&qf)[16], const f32x4& w) {
;     f32x16 p0 = f32x16{}, p1 = f32x16{};
; #pragma unroll
;     for (int d0 = 0; d0 < 4; ++d0) p0 = __builtin_amdgcn_mfma_f32_32x32x16_bf16(kf[d0], qf[d0], p0, 0, 0, 0);
; #pragma unroll
;     for (int d0 = 0; d0 < 4; ++d0) p1 = __builtin_amdgcn_mfma_f32_32x32x16_bf16(kf[d0], qf[4 + d0], p1, 0, 0, 0);
; #pragma unroll
;     for (int r = 0; r < 16; ++r) sc[r] = w[0] * relu_i(p0[r]);
;     p0 = f32x16{};
; #pragma unroll
;     for (int d0 = 0; d0 < 4; ++d0) p0 = __builtin_amdgcn_mfma_f32_32x32x16_bf16(kf[d0], qf[8 + d0], p0, 0, 0, 0);
; #pragma unroll
;     for (int r = 0; r < 16; ++r) sc[r] = fmaf(w[1], relu_i(p1[r]), sc[r]);
;     p1 = f32x16{};
; #pragma unroll
;     for (int d0 = 0; d0 < 4; ++d0) p1 = __builtin_amdgcn_mfma_f32_32x32x16_bf16(kf[d0], qf[12 + d0], p1, 0, 0, 0);
; template <int PASS> __device__ __forceinline__ void idx_pass(const bf16_t* KIb, const bf16x8 (&qf)[16], const f32x4& w, int jd, int tq, int wid, int r32, int hi, unsigned khi, unsigned klo, bool cand, LAS unsigned char* L) {
;     ...
;     for (; j <= jd; j += 8) {
;         const bool diag = (j == jd);
;         idx_loadk(kB, KIb + (size_t)(j * 64 + 32) * 64, r32, hi);
;         f32x16 sc; idx_scores_k(sc, kA, qf, w);
;         unsigned lo, elo, hw, ehw;
;         if (diag) idx_half<PASS, true>(lo, elo, sc, j * 64, tq, r32, hi, khi, klo, cand, L); else idx_half<PASS, false>(lo, elo, sc, j * 64, tq, r32, hi, khi, klo, cand, L);
;         if (j + 8 <= jd) idx_loadk(kA, KIb + (size_t)((j + 8) * 64) * 64, r32, hi);
;         idx_scores_k(sc, kB, qf, w);
;         if (diag) idx_half<PASS, true>(hw, ehw, sc, j * 64 + 32, tq, r32, hi, khi, klo, cand, L); else idx_half<PASS, false>(hw, ehw, sc, j * 64 + 32, tq, r32, hi, khi, klo, cand, L);
.LBB0_750:
	s_and_b64 vcc, exec, s[14:15]
	s_waitcnt vmcnt(3)
	v_mfma_f32_32x32x16_bf16 v[2:17], v[46:49], v[70:73], 0
	s_waitcnt vmcnt(2)
	v_mfma_f32_32x32x16_bf16 v[2:17], v[42:45], v[74:77], v[2:17]
	s_waitcnt vmcnt(1)
	v_mfma_f32_32x32x16_bf16 v[2:17], v[38:41], v[78:81], v[2:17]
	s_waitcnt vmcnt(0)
	v_mfma_f32_32x32x16_bf16 v[2:17], v[34:37], v[82:85], v[2:17]
	v_mfma_f32_32x32x16_bf16 v[180:195], v[46:49], v[86:89], 0
	v_mfma_f32_32x32x16_bf16 v[180:195], v[42:45], v[90:93], v[180:195]
	v_mfma_f32_32x32x16_bf16 v[180:195], v[38:41], v[94:97], v[180:195]
	v_mfma_f32_32x32x16_bf16 v[180:195], v[34:37], v[98:101], v[180:195]
	s_nop 7
	v_max_i32_e32 v200, 0, v2
	v_fma_f32 v136, v66, v200, 0
	v_max_i32_e32 v200, 0, v3
	v_fma_f32 v135, v66, v200, 0
	v_max_i32_e32 v200, 0, v4
	v_fma_f32 v134, v66, v200, 0
	v_max_i32_e32 v200, 0, v5
	v_fma_f32 v65, v66, v200, 0
	v_max_i32_e32 v200, 0, v6
	v_fma_f32 v64, v66, v200, 0
	v_max_i32_e32 v200, 0, v7
	v_fma_f32 v63, v66, v200, 0
	v_max_i32_e32 v200, 0, v8
	v_fma_f32 v62, v66, v200, 0
	v_max_i32_e32 v200, 0, v9
	v_fma_f32 v61, v66, v200, 0
	v_max_i32_e32 v200, 0, v10
	v_fma_f32 v60, v66, v200, 0
	v_max_i32_e32 v200, 0, v11
	v_fma_f32 v59, v66, v200, 0
	v_max_i32_e32 v200, 0, v12
	v_fma_f32 v58, v66, v200, 0
	v_max_i32_e32 v200, 0, v13
	v_fma_f32 v57, v66, v200, 0
	v_max_i32_e32 v200, 0, v14
	v_fma_f32 v56, v66, v200, 0
	v_max_i32_e32 v200, 0, v15
	v_fma_f32 v55, v66, v200, 0
	v_max_i32_e32 v200, 0, v16
	v_fma_f32 v54, v66, v200, 0
	v_max_i32_e32 v200, 0, v17
	v_fma_f32 v53, v66, v200, 0
	v_mfma_f32_32x32x16_bf16 v[2:17], v[46:49], v[102:105], 0
	v_mfma_f32_32x32x16_bf16 v[2:17], v[42:45], v[106:109], v[2:17]
	v_mfma_f32_32x32x16_bf16 v[2:17], v[38:41], v[110:113], v[2:17]
	v_mfma_f32_32x32x16_bf16 v[2:17], v[34:37], v[114:117], v[2:17]
	v_max_i32_e32 v200, 0, v180
	v_fmac_f32_e32 v136, v67, v200
	v_max_i32_e32 v200, 0, v181
	v_fmac_f32_e32 v135, v67, v200
	v_max_i32_e32 v200, 0, v182
	v_fmac_f32_e32 v134, v67, v200
	v_max_i32_e32 v200, 0, v183
	v_fmac_f32_e32 v65, v67, v200
	v_max_i32_e32 v200, 0, v184
	v_fmac_f32_e32 v64, v67, v200
	v_max_i32_e32 v200, 0, v185
	v_fmac_f32_e32 v63, v67, v200
	v_max_i32_e32 v200, 0, v186
	v_fmac_f32_e32 v62, v67, v200
	v_max_i32_e32 v200, 0, v187
	v_fmac_f32_e32 v61, v67, v200
	v_max_i32_e32 v200, 0, v188
	v_fmac_f32_e32 v60, v67, v200
	v_max_i32_e32 v200, 0, v189
	v_fmac_f32_e32 v59, v67, v200
	v_max_i32_e32 v200, 0, v190
	v_fmac_f32_e32 v58, v67, v200
	v_max_i32_e32 v200, 0, v191
	v_fmac_f32_e32 v57, v67, v200
	v_max_i32_e32 v200, 0, v192
	v_fmac_f32_e32 v56, v67, v200
	v_max_i32_e32 v200, 0, v193
	v_fmac_f32_e32 v55, v67, v200
	v_max_i32_e32 v200, 0, v194
	v_fmac_f32_e32 v54, v67, v200
	v_max_i32_e32 v200, 0, v195
	v_fmac_f32_e32 v53, v67, v200
	v_mfma_f32_32x32x16_bf16 v[180:195], v[46:49], v[118:121], 0
	v_mfma_f32_32x32x16_bf16 v[180:195], v[42:45], v[122:125], v[180:195]
	v_mfma_f32_32x32x16_bf16 v[180:195], v[38:41], v[126:129], v[180:195]
	v_mfma_f32_32x32x16_bf16 v[180:195], v[34:37], v[130:133], v[180:195]
	s_cmp_gt_i32 s20, s65
	s_cbranch_scc1 .Lka_p1_skip
	s_ashr_i32 s11, s10, 31
	s_lshl_b64 s[0:1], s[10:11], 7
	v_lshl_add_u64 v[196:197], v[50:51], 0, s[0:1]
	global_load_dwordx4 v[18:21], v[196:197], off
	global_load_dwordx4 v[22:25], v[196:197], off offset:32
	global_load_dwordx4 v[26:29], v[196:197], off offset:64
	global_load_dwordx4 v[30:33], v[196:197], off offset:96
; #define LAS __attribute__((address_space(3)))
; __device__ __forceinline__ int crow(int r, int hi) { return (r & 3) + 8 * (r >> 2) + 4 * hi; }
; __device__ __forceinline__ float relu_i(float p) { const int i = __float_as_int(p); return __int_as_float(i > 0 ? i : 0); }
; __device__ __forceinline__ void idx_scores_k(f32x16& sc, const bf16x8 (&kf)[4], const bf16x8 (&qf)[16], const f32x4& w) {
;     ...
;     for (int d0 = 0; d0 < 4; ++d0) p1 = __builtin_amdgcn_mfma_f32_32x32x16_bf16(kf[d0], qf[12 + d0], p1, 0, 0, 0);
; #pragma unroll
;     for (int r = 0; r < 16; ++r) sc[r] = fmaf(w[2], relu_i(p0[r]), sc[r]);
; #pragma unroll
;     for (int r = 0; r < 16; ++r) sc[r] = fmaf(w[3], relu_i(p1[r]), sc[r]);
; }
; template <int PASS, bool DIAG> __device__ __forceinline__ void idx_half(unsigned& bits, unsigned& ebits, const f32x16& sc, int sbase, int tq, int r32, int hi, unsigned khi, unsigned klo, bool cand, LAS unsigned char* L) {
;     bits = 0u; ebits = 0u;
;     const int d = tq - sbase - 4 * hi;
;     if (PASS == 1) {
;         LAS unsigned* H = (LAS unsigned*)(L + IL_HIST) + r32 * HSTR + 160;
; #pragma unroll
;         for (int r = 0; r < 16; ++r) { int b = ibin_u_m160(__float_as_uint(sc[r] + 0.0f)); asm("" : "+v"(b));
;             if (!DIAG || crow(r, 0) <= d) __hip_atomic_fetch_add(H + b, 1u, __ATOMIC_RELAXED, __HIP_MEMORY_SCOPE_WORKGROUP); }
.Lka_p1_skip:
	v_max_i32_e32 v200, 0, v2
	v_fmac_f32_e32 v136, v68, v200
	v_max_i32_e32 v200, 0, v3
	v_fmac_f32_e32 v135, v68, v200
	v_max_i32_e32 v200, 0, v4
	v_fmac_f32_e32 v134, v68, v200
	v_max_i32_e32 v200, 0, v5
	v_fmac_f32_e32 v65, v68, v200
	v_max_i32_e32 v200, 0, v6
	v_fmac_f32_e32 v64, v68, v200
	v_max_i32_e32 v200, 0, v7
	v_fmac_f32_e32 v63, v68, v200
	v_max_i32_e32 v200, 0, v8
	v_fmac_f32_e32 v62, v68, v200
	v_max_i32_e32 v200, 0, v9
	v_fmac_f32_e32 v61, v68, v200
	v_max_i32_e32 v200, 0, v10
	v_fmac_f32_e32 v60, v68, v200
	v_max_i32_e32 v200, 0, v11
	v_fmac_f32_e32 v59, v68, v200
	v_max_i32_e32 v200, 0, v12
	v_fmac_f32_e32 v58, v68, v200
	v_max_i32_e32 v200, 0, v13
	v_fmac_f32_e32 v57, v68, v200
	v_max_i32_e32 v200, 0, v14
	v_fmac_f32_e32 v56, v68, v200
	v_max_i32_e32 v200, 0, v15
	v_fmac_f32_e32 v55, v68, v200
	v_max_i32_e32 v200, 0, v16
	v_fmac_f32_e32 v54, v68, v200
	v_max_i32_e32 v200, 0, v17
	v_fmac_f32_e32 v53, v68, v200
	v_max_i32_e32 v200, 0, v180
	v_fmac_f32_e32 v136, v69, v200
	v_max_i32_e32 v200, 0, v181
	v_fmac_f32_e32 v135, v69, v200
	v_max_i32_e32 v200, 0, v182
	v_fmac_f32_e32 v134, v69, v200
	v_max_i32_e32 v200, 0, v183
	v_fmac_f32_e32 v65, v69, v200
	v_max_i32_e32 v200, 0, v184
	v_fmac_f32_e32 v64, v69, v200
	v_max_i32_e32 v200, 0, v185
	v_fmac_f32_e32 v63, v69, v200
	v_max_i32_e32 v200, 0, v186
	v_fmac_f32_e32 v62, v69, v200
	v_max_i32_e32 v200, 0, v187
	v_fmac_f32_e32 v61, v69, v200
	v_max_i32_e32 v200, 0, v188
	v_fmac_f32_e32 v60, v69, v200
	v_max_i32_e32 v200, 0, v189
	v_fmac_f32_e32 v59, v69, v200
	v_max_i32_e32 v200, 0, v190
	v_fmac_f32_e32 v58, v69, v200
	v_max_i32_e32 v200, 0, v191
	v_fmac_f32_e32 v57, v69, v200
	v_max_i32_e32 v200, 0, v192
	v_fmac_f32_e32 v56, v69, v200
	v_max_i32_e32 v200, 0, v193
	v_fmac_f32_e32 v55, v69, v200
	v_max_i32_e32 v200, 0, v194
	v_fmac_f32_e32 v54, v69, v200
	v_max_i32_e32 v200, 0, v195
	v_fmac_f32_e32 v53, v69, v200
	s_cbranch_vccz .LBB0_752
	v_ashrrev_i32_e32 v3, 20, v136
	v_sub_u32_e32 v4, 0xfffffc47, v3
	v_med3_i32 v3, v3, s88, v233
	v_med3_i32 v2, v136, s89, 1
	v_med3_i32 v4, v4, 0, v232
	v_add3_u32 v2, v2, v3, v4
	v_lshl_add_u32 v2, v2, 2, v234
	ds_add_u32 v2, v229 offset:1152
	v_ashrrev_i32_e32 v3, 20, v135
	v_sub_u32_e32 v4, 0xfffffc47, v3
	v_med3_i32 v3, v3, s88, v233
	v_med3_i32 v2, v135, s89, 1
	v_med3_i32 v4, v4, 0, v232
	v_add_u32_e32 v2, v2, v3
	v_add3_u32 v2, v2, v4, s92
	s_mov_b64 s[14:15], -1
	v_lshl_add_u32 v2, v2, 2, v0
	ds_add_u32 v2, v229 offset:1152
	v_ashrrev_i32_e32 v3, 20, v134
	v_sub_u32_e32 v4, 0xfffffc47, v3
	v_med3_i32 v3, v3, s88, v233
	v_med3_i32 v2, v134, s89, 1
	v_med3_i32 v4, v4, 0, v232
	v_add3_u32 v2, v2, v3, v4
	v_lshl_add_u32 v2, v2, 2, v234
	ds_add_u32 v2, v229 offset:1152
	v_ashrrev_i32_e32 v3, 20, v65
	v_sub_u32_e32 v4, 0xfffffc47, v3
	v_med3_i32 v3, v3, s88, v233
	v_med3_i32 v2, v65, s89, 1
	v_med3_i32 v4, v4, 0, v232
	v_add3_u32 v2, v2, v3, v4
	v_lshl_add_u32 v2, v2, 2, v234
	ds_add_u32 v2, v229 offset:1152
	v_ashrrev_i32_e32 v3, 20, v64
	v_sub_u32_e32 v4, 0xfffffc47, v3
	v_med3_i32 v3, v3, s88, v233
	v_med3_i32 v2, v64, s89, 1
	v_med3_i32 v4, v4, 0, v232
	v_add3_u32 v2, v2, v3, v4
	v_lshl_add_u32 v2, v2, 2, v234
	ds_add_u32 v2, v229 offset:1152
	v_ashrrev_i32_e32 v3, 20, v63
	v_sub_u32_e32 v4, 0xfffffc47, v3
	v_med3_i32 v3, v3, s88, v233
	v_med3_i32 v2, v63, s89, 1
	v_med3_i32 v4, v4, 0, v232
	v_add3_u32 v2, v2, v3, v4
	v_lshl_add_u32 v2, v2, 2, v234
	ds_add_u32 v2, v229 offset:1152
	v_ashrrev_i32_e32 v3, 20, v62
	v_sub_u32_e32 v4, 0xfffffc47, v3
	v_med3_i32 v3, v3, s88, v233
	v_med3_i32 v2, v62, s89, 1
	v_med3_i32 v4, v4, 0, v232
	v_add3_u32 v2, v2, v3, v4
	v_lshl_add_u32 v2, v2, 2, v234
	ds_add_u32 v2, v229 offset:1152
	v_ashrrev_i32_e32 v3, 20, v61
	v_sub_u32_e32 v4, 0xfffffc47, v3
	v_med3_i32 v3, v3, s88, v233
	v_med3_i32 v2, v61, s89, 1
	v_med3_i32 v4, v4, 0, v232
	v_add3_u32 v2, v2, v3, v4
	v_lshl_add_u32 v2, v2, 2, v234
	ds_add_u32 v2, v229 offset:1152
	v_ashrrev_i32_e32 v3, 20, v60
	v_sub_u32_e32 v4, 0xfffffc47, v3
	v_med3_i32 v3, v3, s88, v233
	v_med3_i32 v2, v60, s89, 1
	v_med3_i32 v4, v4, 0, v232
	v_add3_u32 v2, v2, v3, v4
	v_lshl_add_u32 v2, v2, 2, v234
	ds_add_u32 v2, v229 offset:1152
	v_ashrrev_i32_e32 v3, 20, v59
	v_sub_u32_e32 v4, 0xfffffc47, v3
	v_med3_i32 v3, v3, s88, v233
	v_med3_i32 v2, v59, s89, 1
	v_med3_i32 v4, v4, 0, v232
	v_add3_u32 v2, v2, v3, v4
	v_lshl_add_u32 v2, v2, 2, v234
	ds_add_u32 v2, v229 offset:1152
	v_ashrrev_i32_e32 v3, 20, v58
	v_sub_u32_e32 v4, 0xfffffc47, v3
	v_med3_i32 v3, v3, s88, v233
	v_med3_i32 v2, v58, s89, 1
	v_med3_i32 v4, v4, 0, v232
	v_add3_u32 v2, v2, v3, v4
	v_lshl_add_u32 v2, v2, 2, v234
	ds_add_u32 v2, v229 offset:1152
	v_ashrrev_i32_e32 v3, 20, v57
	v_sub_u32_e32 v4, 0xfffffc47, v3
	v_med3_i32 v3, v3, s88, v233
	v_med3_i32 v2, v57, s89, 1
	v_med3_i32 v4, v4, 0, v232
	v_add3_u32 v2, v2, v3, v4
	v_lshl_add_u32 v2, v2, 2, v234
	ds_add_u32 v2, v229 offset:1152
	v_ashrrev_i32_e32 v3, 20, v56
	v_sub_u32_e32 v4, 0xfffffc47, v3
	v_med3_i32 v3, v3, s88, v233
	v_med3_i32 v2, v56, s89, 1
	v_med3_i32 v4, v4, 0, v232
	v_add3_u32 v2, v2, v3, v4
	v_lshl_add_u32 v2, v2, 2, v234
	ds_add_u32 v2, v229 offset:1152
	v_ashrrev_i32_e32 v3, 20, v55
	v_sub_u32_e32 v4, 0xfffffc47, v3
	v_med3_i32 v3, v3, s88, v233
	v_med3_i32 v2, v55, s89, 1
	v_med3_i32 v4, v4, 0, v232
	v_add3_u32 v2, v2, v3, v4
	v_lshl_add_u32 v2, v2, 2, v234
	ds_add_u32 v2, v229 offset:1152
	v_ashrrev_i32_e32 v3, 20, v54
	v_sub_u32_e32 v4, 0xfffffc47, v3
	v_med3_i32 v3, v3, s88, v233
	v_med3_i32 v2, v54, s89, 1
	v_med3_i32 v4, v4, 0, v232
	v_add3_u32 v2, v2, v3, v4
	v_lshl_add_u32 v2, v2, 2, v234
	ds_add_u32 v2, v229 offset:1152
	v_ashrrev_i32_e32 v3, 20, v53
	v_sub_u32_e32 v4, 0xfffffc47, v3
	v_med3_i32 v3, v3, s88, v233
	v_med3_i32 v2, v53, s89, 1
	v_med3_i32 v4, v4, 0, v232
	v_add_u32_e32 v2, v2, v3
	v_add3_u32 v3, v2, v4, s92
	s_cbranch_execz .LBB0_753
	s_branch .LBB0_784

; __device__ __forceinline__ float relu_i(float p) { const int i = __float_as_int(p); return __int_as_float(i > 0 ? i : 0); }
; __device__ __forceinline__ void idx_scores_k(f32x16& sc, const bf16x8 (&kf)[4], const bf16x8 (&qf)[16], const f32x4& w) {
;     f32x16 p0 = f32x16{}, p1 = f32x16{};
; #pragma unroll
;     for (int d0 = 0; d0 < 4; ++d0) p0 = __builtin_amdgcn_mfma_f32_32x32x16_bf16(kf[d0], qf[d0], p0, 0, 0, 0);
; #pragma unroll
;     for (int d0 = 0; d0 < 4; ++d0) p1 = __builtin_amdgcn_mfma_f32_32x32x16_bf16(kf[d0], qf[4 + d0], p1, 0, 0, 0);
; #pragma unroll
;     for (int r = 0; r < 16; ++r) sc[r] = w[0] * relu_i(p0[r]);
;     p0 = f32x16{};
; #pragma unroll
;     for (int d0 = 0; d0 < 4; ++d0) p0 = __builtin_amdgcn_mfma_f32_32x32x16_bf16(kf[d0], qf[8 + d0], p0, 0, 0, 0);
; #pragma unroll
;     for (int r = 0; r < 16; ++r) sc[r] = fmaf(w[1], relu_i(p1[r]), sc[r]);
;     p1 = f32x16{};
; #pragma unroll
;     for (int d0 = 0; d0 < 4; ++d0) p1 = __builtin_amdgcn_mfma_f32_32x32x16_bf16(kf[d0], qf[12 + d0], p1, 0, 0, 0);
; template <int PASS> __device__ __forceinline__ void idx_pass(const bf16_t* KIb, const bf16x8 (&qf)[16], const f32x4& w, int jd, int tq, int wid, int r32, int hi, unsigned khi, unsigned klo, bool cand, LAS unsigned char* L) {
;     ...
;     for (; j <= jd; j += 8) {
;         const bool diag = (j == jd);
;         idx_loadk(kB, KIb + (size_t)(j * 64 + 32) * 64, r32, hi);
;         f32x16 sc; idx_scores_k(sc, kA, qf, w);
;         unsigned lo, elo, hw, ehw;
;         if (diag) idx_half<PASS, true>(lo, elo, sc, j * 64, tq, r32, hi, khi, klo, cand, L); else idx_half<PASS, false>(lo, elo, sc, j * 64, tq, r32, hi, khi, klo, cand, L);
;         if (j + 8 <= jd) idx_loadk(kA, KIb + (size_t)((j + 8) * 64) * 64, r32, hi);
;         idx_scores_k(sc, kB, qf, w);
;         if (diag) idx_half<PASS, true>(hw, ehw, sc, j * 64 + 32, tq, r32, hi, khi, klo, cand, L); else idx_half<PASS, false>(hw, ehw, sc, j * 64 + 32, tq, r32, hi, khi, klo, cand, L);
.LBB0_1130:
.LBB0_1131:
	s_mov_b64 s[14:15], -1
	s_and_b64 vcc, exec, s[18:19]
	s_waitcnt vmcnt(3)
	v_mfma_f32_32x32x16_bf16 v[2:17], v[46:49], v[70:73], 0
	s_waitcnt vmcnt(2)
	v_mfma_f32_32x32x16_bf16 v[2:17], v[42:45], v[74:77], v[2:17]
	s_waitcnt vmcnt(1)
	v_mfma_f32_32x32x16_bf16 v[2:17], v[38:41], v[78:81], v[2:17]
	s_waitcnt vmcnt(0)
	v_mfma_f32_32x32x16_bf16 v[2:17], v[34:37], v[82:85], v[2:17]
	v_mfma_f32_32x32x16_bf16 v[180:195], v[46:49], v[86:89], 0
	v_mfma_f32_32x32x16_bf16 v[180:195], v[42:45], v[90:93], v[180:195]
	v_mfma_f32_32x32x16_bf16 v[180:195], v[38:41], v[94:97], v[180:195]
	v_mfma_f32_32x32x16_bf16 v[180:195], v[34:37], v[98:101], v[180:195]
	s_nop 7
	v_max_i32_e32 v200, 0, v2
	v_fma_f32 v53, v66, v200, 0
	v_max_i32_e32 v200, 0, v3
	v_fma_f32 v54, v66, v200, 0
	v_max_i32_e32 v200, 0, v4
	v_fma_f32 v55, v66, v200, 0
	v_max_i32_e32 v200, 0, v5
	v_fma_f32 v56, v66, v200, 0
	v_max_i32_e32 v200, 0, v6
	v_fma_f32 v57, v66, v200, 0
	v_max_i32_e32 v200, 0, v7
	v_fma_f32 v58, v66, v200, 0
	v_max_i32_e32 v200, 0, v8
	v_fma_f32 v59, v66, v200, 0
	v_max_i32_e32 v200, 0, v9
	v_fma_f32 v60, v66, v200, 0
	v_max_i32_e32 v200, 0, v10
	v_fma_f32 v61, v66, v200, 0
	v_max_i32_e32 v200, 0, v11
	v_fma_f32 v62, v66, v200, 0
	v_max_i32_e32 v200, 0, v12
	v_fma_f32 v63, v66, v200, 0
	v_max_i32_e32 v200, 0, v13
	v_fma_f32 v64, v66, v200, 0
	v_max_i32_e32 v200, 0, v14
	v_fma_f32 v65, v66, v200, 0
	v_max_i32_e32 v200, 0, v15
	v_fma_f32 v144, v66, v200, 0
	v_max_i32_e32 v200, 0, v16
	v_fma_f32 v145, v66, v200, 0
	v_max_i32_e32 v200, 0, v17
	v_fma_f32 v146, v66, v200, 0
	v_mfma_f32_32x32x16_bf16 v[2:17], v[46:49], v[102:105], 0
	v_mfma_f32_32x32x16_bf16 v[2:17], v[42:45], v[106:109], v[2:17]
	v_mfma_f32_32x32x16_bf16 v[2:17], v[38:41], v[110:113], v[2:17]
	v_mfma_f32_32x32x16_bf16 v[2:17], v[34:37], v[114:117], v[2:17]
	v_max_i32_e32 v200, 0, v180
	v_fmac_f32_e32 v53, v67, v200
	v_max_i32_e32 v200, 0, v181
	v_fmac_f32_e32 v54, v67, v200
	v_max_i32_e32 v200, 0, v182
	v_fmac_f32_e32 v55, v67, v200
	v_max_i32_e32 v200, 0, v183
	v_fmac_f32_e32 v56, v67, v200
	v_max_i32_e32 v200, 0, v184
	v_fmac_f32_e32 v57, v67, v200
	v_max_i32_e32 v200, 0, v185
	v_fmac_f32_e32 v58, v67, v200
	v_max_i32_e32 v200, 0, v186
	v_fmac_f32_e32 v59, v67, v200
	v_max_i32_e32 v200, 0, v187
	v_fmac_f32_e32 v60, v67, v200
	v_max_i32_e32 v200, 0, v188
	v_fmac_f32_e32 v61, v67, v200
	v_max_i32_e32 v200, 0, v189
	v_fmac_f32_e32 v62, v67, v200
	v_max_i32_e32 v200, 0, v190
	v_fmac_f32_e32 v63, v67, v200
	v_max_i32_e32 v200, 0, v191
	v_fmac_f32_e32 v64, v67, v200
	v_max_i32_e32 v200, 0, v192
	v_fmac_f32_e32 v65, v67, v200
	v_max_i32_e32 v200, 0, v193
	v_fmac_f32_e32 v144, v67, v200
	v_max_i32_e32 v200, 0, v194
	v_fmac_f32_e32 v145, v67, v200
	v_max_i32_e32 v200, 0, v195
	v_fmac_f32_e32 v146, v67, v200
	v_mfma_f32_32x32x16_bf16 v[180:195], v[46:49], v[118:121], 0
	v_mfma_f32_32x32x16_bf16 v[180:195], v[42:45], v[122:125], v[180:195]
	v_mfma_f32_32x32x16_bf16 v[180:195], v[38:41], v[126:129], v[180:195]
	v_mfma_f32_32x32x16_bf16 v[180:195], v[34:37], v[130:133], v[180:195]
	s_cmp_gt_i32 s44, s65
	s_cbranch_scc1 .Lka_p2_skip
	s_ashr_i32 s17, s16, 31
	s_lshl_b64 s[0:1], s[16:17], 7
	v_lshl_add_u64 v[196:197], v[50:51], 0, s[0:1]
	global_load_dwordx4 v[18:21], v[196:197], off
	global_load_dwordx4 v[22:25], v[196:197], off offset:32
	global_load_dwordx4 v[26:29], v[196:197], off offset:64
	global_load_dwordx4 v[30:33], v[196:197], off offset:96
; #define LAS __attribute__((address_space(3)))
; __device__ __forceinline__ int crow(int r, int hi) { return (r & 3) + 8 * (r >> 2) + 4 * hi; }
; __device__ __forceinline__ unsigned fkey2(float v) { const unsigned u = __float_as_uint(v + 0.0f); return u ^ ((unsigned)((int)u >> 31) | 0x80000000u); }
; __device__ __forceinline__ void idx_scores_k(f32x16& sc, const bf16x8 (&kf)[4], const bf16x8 (&qf)[16], const f32x4& w) {
;     ...
;     for (int d0 = 0; d0 < 4; ++d0) p1 = __builtin_amdgcn_mfma_f32_32x32x16_bf16(kf[d0], qf[12 + d0], p1, 0, 0, 0);
; #pragma unroll
;     for (int r = 0; r < 16; ++r) sc[r] = fmaf(w[2], relu_i(p0[r]), sc[r]);
; #pragma unroll
;     for (int r = 0; r < 16; ++r) sc[r] = fmaf(w[3], relu_i(p1[r]), sc[r]);
; }
; template <int PASS, bool DIAG> __device__ __forceinline__ void idx_half(unsigned& bits, unsigned& ebits, const f32x16& sc, int sbase, int tq, int r32, int hi, unsigned khi, unsigned klo, bool cand, LAS unsigned char* L) {
;     bits = 0u; ebits = 0u;
;     const int d = tq - sbase - 4 * hi;
;     if (PASS == 1) {
;         LAS unsigned* H = (LAS unsigned*)(L + IL_HIST) + r32 * HSTR + 160;
; #pragma unroll
;         for (int r = 0; r < 16; ++r) { int b = ibin_u_m160(__float_as_uint(sc[r] + 0.0f)); asm("" : "+v"(b));
;             if (!DIAG || crow(r, 0) <= d) __hip_atomic_fetch_add(H + b, 1u, __ATOMIC_RELAXED, __HIP_MEMORY_SCOPE_WORKGROUP); }
;     } else {
;         unsigned hb = 0u, lb = 0u;
; #pragma unroll
;         for (int r = 15; r >= 0; --r) { const unsigned key = fkey2(sc[r]); shl_ge(hb, key, khi); shl_ge(lb, key, klo); }
;         bits = spread4(hb); ebits = spread4(lb & ~hb);
;         if (DIAG) { const unsigned vm = d < 0 ? 0u : (d >= 31 ? 0xFFFFFFFFu : ((2u << d) - 1u)); bits &= vm; ebits &= vm; }
;         if (cand && ebits != 0u) {
;             unsigned slot = __hip_atomic_fetch_add((LAS unsigned*)(L + IL_CNT) + r32, (unsigned)__builtin_popcount(ebits), __ATOMIC_RELAXED, __HIP_MEMORY_SCOPE_WORKGROUP);
; #pragma unroll
;             for (int r = 0; r < 16; ++r) if ((ebits >> crow(r, 0)) & 1u) { const int s = sbase + crow(r, hi);
;                 if (slot < (unsigned)IDX_CAP) ((LAS unsigned long long*)(L + IL_CAND))[r32 * IDX_CAP + slot] = ((unsigned long long)fkey2(sc[r]) << 16) | (unsigned long long)(0xFFFFu - (unsigned)s);
;                 ++slot; }
.Lka_p2_skip:
	v_max_i32_e32 v200, 0, v2
	v_fmac_f32_e32 v53, v68, v200
	v_max_i32_e32 v200, 0, v3
	v_fmac_f32_e32 v54, v68, v200
	v_max_i32_e32 v200, 0, v4
	v_fmac_f32_e32 v55, v68, v200
	v_max_i32_e32 v200, 0, v5
	v_fmac_f32_e32 v56, v68, v200
	v_max_i32_e32 v200, 0, v6
	v_fmac_f32_e32 v57, v68, v200
	v_max_i32_e32 v200, 0, v7
	v_fmac_f32_e32 v58, v68, v200
	v_max_i32_e32 v200, 0, v8
	v_fmac_f32_e32 v59, v68, v200
	v_max_i32_e32 v200, 0, v9
	v_fmac_f32_e32 v60, v68, v200
	v_max_i32_e32 v200, 0, v10
	v_fmac_f32_e32 v61, v68, v200
	v_max_i32_e32 v200, 0, v11
	v_fmac_f32_e32 v62, v68, v200
	v_max_i32_e32 v200, 0, v12
	v_fmac_f32_e32 v63, v68, v200
	v_max_i32_e32 v200, 0, v13
	v_fmac_f32_e32 v64, v68, v200
	v_max_i32_e32 v200, 0, v14
	v_fmac_f32_e32 v65, v68, v200
	v_max_i32_e32 v200, 0, v15
	v_fmac_f32_e32 v144, v68, v200
	v_max_i32_e32 v200, 0, v16
	v_fmac_f32_e32 v145, v68, v200
	v_max_i32_e32 v200, 0, v17
	v_fmac_f32_e32 v146, v68, v200
	v_max_i32_e32 v200, 0, v180
	v_fmac_f32_e32 v53, v69, v200
	v_max_i32_e32 v200, 0, v181
	v_fmac_f32_e32 v54, v69, v200
	v_max_i32_e32 v200, 0, v182
	v_fmac_f32_e32 v55, v69, v200
	v_max_i32_e32 v200, 0, v183
	v_fmac_f32_e32 v56, v69, v200
	v_max_i32_e32 v200, 0, v184
	v_fmac_f32_e32 v57, v69, v200
	v_max_i32_e32 v200, 0, v185
	v_fmac_f32_e32 v58, v69, v200
	v_max_i32_e32 v200, 0, v186
	v_fmac_f32_e32 v59, v69, v200
	v_max_i32_e32 v200, 0, v187
	v_fmac_f32_e32 v60, v69, v200
	v_max_i32_e32 v200, 0, v188
	v_fmac_f32_e32 v61, v69, v200
	v_max_i32_e32 v200, 0, v189
	v_fmac_f32_e32 v62, v69, v200
	v_max_i32_e32 v200, 0, v190
	v_fmac_f32_e32 v63, v69, v200
	v_max_i32_e32 v200, 0, v191
	v_fmac_f32_e32 v64, v69, v200
	v_max_i32_e32 v200, 0, v192
	v_fmac_f32_e32 v65, v69, v200
	v_max_i32_e32 v200, 0, v193
	v_fmac_f32_e32 v144, v69, v200
	v_max_i32_e32 v200, 0, v194
	v_fmac_f32_e32 v145, v69, v200
	v_max_i32_e32 v200, 0, v195
	v_fmac_f32_e32 v146, v69, v200
	s_cbranch_vccz .LBB0_1196
	v_mov_b32_e32 v49, 0
	v_mov_b32_e32 v5, 0
	v_cmp_ge_f32 vcc, v146, v165
	v_addc_co_u32 v49, vcc, v49, v49, vcc
	v_cmp_ge_f32 vcc, v146, v164
	v_addc_co_u32 v5, vcc, v5, v5, vcc
	v_cmp_ge_f32 vcc, v145, v165
	v_addc_co_u32 v49, vcc, v49, v49, vcc
	v_cmp_ge_f32 vcc, v145, v164
	v_addc_co_u32 v5, vcc, v5, v5, vcc
	v_cmp_ge_f32 vcc, v144, v165
	v_addc_co_u32 v49, vcc, v49, v49, vcc
	v_cmp_ge_f32 vcc, v144, v164
	v_addc_co_u32 v5, vcc, v5, v5, vcc
	v_cmp_ge_f32 vcc, v65, v165
	v_addc_co_u32 v49, vcc, v49, v49, vcc
	v_cmp_ge_f32 vcc, v65, v164
	v_addc_co_u32 v5, vcc, v5, v5, vcc
	v_cmp_ge_f32 vcc, v64, v165
	v_addc_co_u32 v49, vcc, v49, v49, vcc
	v_cmp_ge_f32 vcc, v64, v164
	v_addc_co_u32 v5, vcc, v5, v5, vcc
	v_cmp_ge_f32 vcc, v63, v165
	v_addc_co_u32 v49, vcc, v49, v49, vcc
	v_cmp_ge_f32 vcc, v63, v164
	v_addc_co_u32 v5, vcc, v5, v5, vcc
	v_cmp_ge_f32 vcc, v62, v165
	v_addc_co_u32 v49, vcc, v49, v49, vcc
	v_cmp_ge_f32 vcc, v62, v164
	v_addc_co_u32 v5, vcc, v5, v5, vcc
	v_cmp_ge_f32 vcc, v61, v165
	v_addc_co_u32 v49, vcc, v49, v49, vcc
	v_cmp_ge_f32 vcc, v61, v164
	v_addc_co_u32 v5, vcc, v5, v5, vcc
	v_cmp_ge_f32 vcc, v60, v165
	v_addc_co_u32 v49, vcc, v49, v49, vcc
	v_cmp_ge_f32 vcc, v60, v164
	v_addc_co_u32 v5, vcc, v5, v5, vcc
	v_cmp_ge_f32 vcc, v59, v165
	v_addc_co_u32 v49, vcc, v49, v49, vcc
	v_cmp_ge_f32 vcc, v59, v164
	v_addc_co_u32 v5, vcc, v5, v5, vcc
	v_cmp_ge_f32 vcc, v58, v165
	v_addc_co_u32 v49, vcc, v49, v49, vcc
	v_cmp_ge_f32 vcc, v58, v164
	v_addc_co_u32 v5, vcc, v5, v5, vcc
	v_cmp_ge_f32 vcc, v57, v165
	v_addc_co_u32 v49, vcc, v49, v49, vcc
	v_cmp_ge_f32 vcc, v57, v164
	v_addc_co_u32 v5, vcc, v5, v5, vcc
	s_nop 0
	v_cmp_ge_f32 vcc, v56, v165
	v_addc_co_u32 v49, vcc, v49, v49, vcc
	s_nop 0
	v_cmp_ge_f32 vcc, v56, v164
	v_addc_co_u32 v5, vcc, v5, v5, vcc
	s_nop 0
	v_cmp_ge_f32 vcc, v55, v165
	v_addc_co_u32 v49, vcc, v49, v49, vcc
	s_nop 0
	v_cmp_ge_f32 vcc, v55, v164
	v_addc_co_u32 v5, vcc, v5, v5, vcc
	s_nop 0
	v_cmp_ge_f32 vcc, v54, v165
	v_addc_co_u32 v49, vcc, v49, v49, vcc
	s_nop 0
	v_cmp_ge_f32 vcc, v54, v164
	v_addc_co_u32 v5, vcc, v5, v5, vcc
	s_nop 0
	v_cmp_ge_f32 vcc, v53, v165
	v_addc_co_u32 v49, vcc, v49, v49, vcc
	s_nop 0
	v_cmp_ge_f32 vcc, v53, v164
	v_addc_co_u32 v5, vcc, v5, v5, vcc
	s_nop 0
	v_bitop3_b32 v3, v5, v49, v5 bitop3:0x30
	v_bitop3_b32 v5, v5, 15, v49 bitop3:0x40
	v_lshlrev_b32_e32 v7, 4, v3
	v_and_or_b32 v5, v7, s93, v5
	v_lshlrev_b32_e32 v7, 8, v3
	v_lshlrev_b32_e32 v9, 12, v3
	v_and_b32_e32 v7, 0xf0000, v7
	v_and_b32_e32 v9, 0xf000000, v9
	v_or3_b32 v48, v5, v7, v9
	v_cmp_ne_u32_e32 vcc, 0, v48
	s_and_b64 s[0:1], s[10:11], vcc
	s_and_saveexec_b64 s[18:19], s[0:1]
	s_cbranch_execz .LBB0_1195
	v_bcnt_u32_b32 v5, v48, 0
	ds_add_rtn_u32 v147, v221, v5
	v_and_b32_e32 v5, 1, v3
	v_cmp_eq_u32_e32 vcc, 1, v5
	s_and_saveexec_b64 s[14:15], vcc
	s_cbranch_execz .LBB0_1137
	s_waitcnt lgkmcnt(0)
	v_cmp_gt_u32_e32 vcc, s87, v147
	s_and_saveexec_b64 s[42:43], vcc
	s_cbranch_execz .LBB0_1136
	v_add_f32_e32 v0, 0, v53
	v_ashrrev_i32_e32 v252, 31, v0
	v_bitop3_b32 v0, v252, v0, s85 bitop3:0x36
	v_lshlrev_b64 v[148:149], 16, v[0:1]
	v_add_u32_e32 v0, s45, v142
	v_subrev_u32_e32 v0, 32, v0
	v_lshl_add_u32 v5, v147, 3, v136
	v_or_b32_e32 v148, v148, v0
	ds_write_b64 v5, v[148:149] offset:512
